# baseline (speedup 1.0000x reference)
.LBB3_5:
	s_or_b64 exec, exec, s[22:23]
	s_mov_b64 s[4:5], 0x10000
	v_lshl_add_u64 v[90:91], v[2:3], 0, s[4:5]
	s_mov_b64 s[4:5], 0x12000
	v_lshl_add_u64 v[92:93], v[2:3], 0, s[4:5]
	s_mov_b64 s[4:5], 0x14000
	v_lshl_add_u64 v[94:95], v[2:3], 0, s[4:5]
	s_mov_b64 s[4:5], 0x16000
	v_lshl_add_u64 v[96:97], v[2:3], 0, s[4:5]
	s_mov_b64 s[4:5], 0x18000
	v_lshl_add_u64 v[98:99], v[2:3], 0, s[4:5]
	s_mov_b64 s[4:5], 0x1a000
	v_lshl_add_u64 v[100:101], v[2:3], 0, s[4:5]
	s_mov_b64 s[4:5], 0x1c000
	v_lshl_add_u64 v[102:103], v[2:3], 0, s[4:5]
	s_mov_b64 s[4:5], 0x1e000
	v_lshlrev_b32_e32 v89, 4, v1
	v_lshl_add_u64 v[104:105], v[2:3], 0, s[4:5]
	s_mov_b64 s[6:7], 0
	s_mov_b64 s[4:5], -1
	v_mov_b32_e32 v19, v18
	v_mov_b32_e32 v20, v18
	v_mov_b32_e32 v21, v18
	v_mov_b32_e32 v84, v18
	v_mov_b32_e32 v85, v18
	v_mov_b32_e32 v86, v18
	v_mov_b32_e32 v87, v18
	s_waitcnt vmcnt(10)
	ds_write_b128 v88, v[40:43]
	s_waitcnt vmcnt(9)
	ds_write_b128 v88, v[44:47] offset:8192
	s_waitcnt vmcnt(8)
	ds_write_b128 v88, v[48:51] offset:16384
	s_waitcnt vmcnt(7)
	ds_write_b128 v88, v[52:55] offset:24576
	s_waitcnt lgkmcnt(0)
	s_barrier
	v_readfirstlane_b32 s44, v0
	s_nop 3
	s_lshr_b32 s44, s44, 6
	s_cmp_ge_u32 s44, 4
	s_cbranch_scc0 .Lmy_attn_noprio
	s_setprio 1
.Lmy_attn_noprio:
	s_branch .LBB3_7
